# P0: one s_barrier per W1/W2 conversion trip (8 waves of a WG load in lockstep) + E3 residual epilogue batched loads
# speedup vs baseline: 1.0142x; 1.0142x over previous
.LBB0_114:
	s_barrier
	s_add_i32 s10, s8, s2
	s_cmp_gt_i32 s10, 0xffff
	s_cselect_b64 s[6:7], -1, 0
	s_and_b64 vcc, exec, s[6:7]
	s_cbranch_vccnz .LBB0_113
	s_ashr_i32 s9, s10, 31
	s_lshr_b32 s9, s9, 23
	s_add_i32 s9, s10, s9
	s_ashr_i32 s12, s9, 9
	s_ashr_i32 s13, s12, 31
	s_lshl_b64 s[12:13], s[12:13], 23
	s_add_u32 s11, s4, s12
	s_addc_u32 s14, s5, s13
	s_and_b32 s9, s9, 0xfffffe00
	s_sub_i32 s9, s10, s9
	s_ashr_i32 s12, s9, 31
	s_lshr_b32 s12, s12, 26
	s_add_i32 s12, s9, s12
	s_and_b32 s13, s12, 0x7ffffc0
	s_sub_i32 s9, s9, s13
	s_lshl_b32 s12, s12, 1
	s_and_b32 s13, s12, 0xffffff80
	s_lshl_b32 s12, s9, 5
	v_or_b32_e32 v98, s13, v1
	s_ashr_i32 s13, s12, 31
	s_lshl_b64 s[12:13], s[12:13], 2
	s_add_u32 s12, s11, s12
	s_addc_u32 s13, s14, s13
	v_ashrrev_i32_e32 v99, 31, v98
	v_lshl_add_u64 v[100:101], s[12:13], 0, v[136:137]
	v_lshlrev_b64 v[10:11], 13, v[98:99]
	v_lshl_add_u64 v[22:23], v[100:101], 0, v[10:11]
	v_or_b32_e32 v10, 8, v98
	v_ashrrev_i32_e32 v11, 31, v10
	v_lshlrev_b64 v[10:11], 13, v[10:11]
	v_lshl_add_u64 v[24:25], v[100:101], 0, v[10:11]
	global_load_dwordx4 v[14:17], v[22:23], off nt
	global_load_dwordx4 v[10:13], v[24:25], off nt
	v_or_b32_e32 v22, 16, v98
	v_ashrrev_i32_e32 v23, 31, v22
	v_lshlrev_b64 v[22:23], 13, v[22:23]
	v_lshl_add_u64 v[38:39], v[100:101], 0, v[22:23]
	v_or_b32_e32 v22, 24, v98
	v_ashrrev_i32_e32 v23, 31, v22
	v_lshlrev_b64 v[22:23], 13, v[22:23]
	v_lshl_add_u64 v[40:41], v[100:101], 0, v[22:23]
	global_load_dwordx4 v[26:29], v[38:39], off nt
	global_load_dwordx4 v[22:25], v[40:41], off nt
	v_or_b32_e32 v38, 32, v98
	v_ashrrev_i32_e32 v39, 31, v38
	v_lshlrev_b64 v[38:39], 13, v[38:39]
	v_lshl_add_u64 v[46:47], v[100:101], 0, v[38:39]
	v_or_b32_e32 v38, 40, v98
	v_ashrrev_i32_e32 v39, 31, v38
	v_lshlrev_b64 v[38:39], 13, v[38:39]
	v_lshl_add_u64 v[48:49], v[100:101], 0, v[38:39]
	global_load_dwordx4 v[42:45], v[46:47], off nt
	global_load_dwordx4 v[38:41], v[48:49], off nt
	v_or_b32_e32 v46, 48, v98
	v_ashrrev_i32_e32 v47, 31, v46
	v_lshlrev_b64 v[46:47], 13, v[46:47]
	v_lshl_add_u64 v[62:63], v[100:101], 0, v[46:47]
	v_or_b32_e32 v46, 56, v98
	v_ashrrev_i32_e32 v47, 31, v46
	v_lshlrev_b64 v[46:47], 13, v[46:47]
	v_lshl_add_u64 v[64:65], v[100:101], 0, v[46:47]
	global_load_dwordx4 v[50:53], v[62:63], off nt
	global_load_dwordx4 v[46:49], v[64:65], off nt
	v_or_b32_e32 v62, 64, v98
	v_or_b32_e32 v64, 0x48, v98
	v_or_b32_e32 v74, 0x50, v98
	v_or_b32_e32 v76, 0x58, v98
	v_or_b32_e32 v86, 0x60, v98
	v_or_b32_e32 v88, 0x68, v98
	v_or_b32_e32 v102, 0x70, v98
	v_or_b32_e32 v98, 0x78, v98
	v_ashrrev_i32_e32 v63, 31, v62
	v_ashrrev_i32_e32 v65, 31, v64
	v_ashrrev_i32_e32 v75, 31, v74
	v_ashrrev_i32_e32 v77, 31, v76
	v_ashrrev_i32_e32 v87, 31, v86
	v_ashrrev_i32_e32 v89, 31, v88
	v_ashrrev_i32_e32 v103, 31, v102
	v_ashrrev_i32_e32 v99, 31, v98
	v_lshlrev_b64 v[62:63], 13, v[62:63]
	v_lshlrev_b64 v[64:65], 13, v[64:65]
	v_lshlrev_b64 v[74:75], 13, v[74:75]
	v_lshlrev_b64 v[76:77], 13, v[76:77]
	v_lshlrev_b64 v[86:87], 13, v[86:87]
	v_lshlrev_b64 v[88:89], 13, v[88:89]
	v_lshlrev_b64 v[102:103], 13, v[102:103]
	v_lshlrev_b64 v[98:99], 13, v[98:99]
	v_lshl_add_u64 v[62:63], v[100:101], 0, v[62:63]
	v_lshl_add_u64 v[64:65], v[100:101], 0, v[64:65]
	v_lshl_add_u64 v[74:75], v[100:101], 0, v[74:75]
	v_lshl_add_u64 v[76:77], v[100:101], 0, v[76:77]
	v_lshl_add_u64 v[86:87], v[100:101], 0, v[86:87]
	v_lshl_add_u64 v[88:89], v[100:101], 0, v[88:89]
	v_lshl_add_u64 v[102:103], v[100:101], 0, v[102:103]
	v_lshl_add_u64 v[98:99], v[100:101], 0, v[98:99]
	global_load_dwordx4 v[66:69], v[62:63], off nt
	s_nop 0
	global_load_dwordx4 v[62:65], v[64:65], off nt
	s_nop 0
	global_load_dwordx4 v[78:81], v[74:75], off nt
	s_nop 0
	global_load_dwordx4 v[74:77], v[76:77], off nt
	s_nop 0
	global_load_dwordx4 v[90:93], v[86:87], off nt
	s_nop 0
	global_load_dwordx4 v[86:89], v[88:89], off nt
	s_nop 0
	global_load_dwordx4 v[102:105], v[102:103], off nt
	s_nop 0
	global_load_dwordx4 v[98:101], v[98:99], off nt
	s_branch .LBB0_113

.LBB0_119:
	s_barrier
	s_add_i32 s10, s8, s2
	s_cmpk_gt_i32 s10, 0x7fff
	s_cselect_b64 s[6:7], -1, 0
	s_and_b64 vcc, exec, s[6:7]
	s_cbranch_vccnz .LBB0_118
	s_ashr_i32 s9, s10, 31
	s_lshr_b32 s9, s9, 24
	s_add_i32 s9, s10, s9
	s_ashr_i32 s12, s9, 8
	s_ashr_i32 s13, s12, 31
	s_lshl_b64 s[12:13], s[12:13], 22
	s_add_u32 s11, s4, s12
	s_addc_u32 s14, s5, s13
	s_and_b32 s9, s9, 0xffffff00
	s_sub_i32 s9, s10, s9
	s_ashr_i32 s12, s9, 31
	s_lshr_b32 s12, s12, 27
	s_add_i32 s12, s9, s12
	s_and_b32 s13, s12, 0x7ffffe0
	s_sub_i32 s9, s9, s13
	s_lshl_b32 s12, s12, 2
	s_and_b32 s13, s12, 0xffffff80
	s_lshl_b32 s12, s9, 5
	v_or_b32_e32 v102, s13, v1
	s_ashr_i32 s13, s12, 31
	s_lshl_b64 s[12:13], s[12:13], 2
	s_add_u32 s12, s11, s12
	s_addc_u32 s13, s14, s13
	v_ashrrev_i32_e32 v103, 31, v102
	v_lshl_add_u64 v[104:105], s[12:13], 0, v[136:137]
	v_lshlrev_b64 v[14:15], 12, v[102:103]
	v_lshl_add_u64 v[26:27], v[104:105], 0, v[14:15]
	v_or_b32_e32 v14, 8, v102
	v_ashrrev_i32_e32 v15, 31, v14
	v_lshlrev_b64 v[14:15], 12, v[14:15]
	v_lshl_add_u64 v[28:29], v[104:105], 0, v[14:15]
	global_load_dwordx4 v[18:21], v[26:27], off nt
	global_load_dwordx4 v[14:17], v[28:29], off nt
	v_or_b32_e32 v26, 16, v102
	v_ashrrev_i32_e32 v27, 31, v26
	v_lshlrev_b64 v[26:27], 12, v[26:27]
	v_lshl_add_u64 v[38:39], v[104:105], 0, v[26:27]
	v_or_b32_e32 v26, 24, v102
	v_ashrrev_i32_e32 v27, 31, v26
	v_lshlrev_b64 v[26:27], 12, v[26:27]
	v_lshl_add_u64 v[40:41], v[104:105], 0, v[26:27]
	global_load_dwordx4 v[30:33], v[38:39], off nt
	global_load_dwordx4 v[26:29], v[40:41], off nt
	v_or_b32_e32 v38, 32, v102
	v_ashrrev_i32_e32 v39, 31, v38
	v_lshlrev_b64 v[38:39], 12, v[38:39]
	v_lshl_add_u64 v[54:55], v[104:105], 0, v[38:39]
	v_or_b32_e32 v38, 40, v102
	v_ashrrev_i32_e32 v39, 31, v38
	v_lshlrev_b64 v[38:39], 12, v[38:39]
	v_lshl_add_u64 v[56:57], v[104:105], 0, v[38:39]
	global_load_dwordx4 v[42:45], v[54:55], off nt
	global_load_dwordx4 v[38:41], v[56:57], off nt
	v_or_b32_e32 v54, 48, v102
	v_ashrrev_i32_e32 v55, 31, v54
	v_lshlrev_b64 v[54:55], 12, v[54:55]
	v_lshl_add_u64 v[62:63], v[104:105], 0, v[54:55]
	v_or_b32_e32 v54, 56, v102
	v_ashrrev_i32_e32 v55, 31, v54
	v_lshlrev_b64 v[54:55], 12, v[54:55]
	v_lshl_add_u64 v[64:65], v[104:105], 0, v[54:55]
	global_load_dwordx4 v[58:61], v[62:63], off nt
	global_load_dwordx4 v[54:57], v[64:65], off nt
	v_or_b32_e32 v62, 64, v102
	v_ashrrev_i32_e32 v63, 31, v62
	v_lshlrev_b64 v[62:63], 12, v[62:63]
	v_lshl_add_u64 v[78:79], v[104:105], 0, v[62:63]
	v_or_b32_e32 v62, 0x48, v102
	v_ashrrev_i32_e32 v63, 31, v62
	v_lshlrev_b64 v[62:63], 12, v[62:63]
	v_lshl_add_u64 v[80:81], v[104:105], 0, v[62:63]
	global_load_dwordx4 v[66:69], v[78:79], off nt
	global_load_dwordx4 v[62:65], v[80:81], off nt
	v_or_b32_e32 v78, 0x50, v102
	v_or_b32_e32 v80, 0x58, v102
	v_or_b32_e32 v90, 0x60, v102
	v_or_b32_e32 v92, 0x68, v102
	v_or_b32_e32 v106, 0x70, v102
	v_or_b32_e32 v102, 0x78, v102
	v_ashrrev_i32_e32 v79, 31, v78
	v_ashrrev_i32_e32 v81, 31, v80
	v_ashrrev_i32_e32 v91, 31, v90
	v_ashrrev_i32_e32 v93, 31, v92
	v_ashrrev_i32_e32 v107, 31, v106
	v_ashrrev_i32_e32 v103, 31, v102
	v_lshlrev_b64 v[78:79], 12, v[78:79]
	v_lshlrev_b64 v[80:81], 12, v[80:81]
	v_lshlrev_b64 v[90:91], 12, v[90:91]
	v_lshlrev_b64 v[92:93], 12, v[92:93]
	v_lshlrev_b64 v[106:107], 12, v[106:107]
	v_lshlrev_b64 v[102:103], 12, v[102:103]
	v_lshl_add_u64 v[78:79], v[104:105], 0, v[78:79]
	v_lshl_add_u64 v[80:81], v[104:105], 0, v[80:81]
	v_lshl_add_u64 v[90:91], v[104:105], 0, v[90:91]
	v_lshl_add_u64 v[92:93], v[104:105], 0, v[92:93]
	v_lshl_add_u64 v[106:107], v[104:105], 0, v[106:107]
	v_lshl_add_u64 v[102:103], v[104:105], 0, v[102:103]
	global_load_dwordx4 v[82:85], v[78:79], off nt
	s_nop 0
	global_load_dwordx4 v[78:81], v[80:81], off nt
	s_nop 0
	global_load_dwordx4 v[94:97], v[90:91], off nt
	s_nop 0
	global_load_dwordx4 v[90:93], v[92:93], off nt
	s_nop 0
	global_load_dwordx4 v[106:109], v[106:107], off nt
	s_nop 0
	global_load_dwordx4 v[102:105], v[102:103], off nt
	s_branch .LBB0_118
